# P7 epilogue: -log2e folded into the 8 row scales (one multiply per sigmoid argument); P13 loop: dropped a mid-burst lgkmcnt wait
# baseline (speedup 1.0000x reference)
.LBB0_1047:
	s_lshl_b32 s4, s64, 8
	v_mov_b32_e32 v148, v0
	s_add_i32 s4, s4, s58
	s_mov_b32 s12, 0x20000
	v_and_or_b32 v212, v148, 15, s4
	s_lshl_b32 s4, s63, 6
	s_or_b32 s4, s4, s61
	v_lshrrev_b32_e32 v2, 2, v148
	v_and_or_b32 v214, v2, 12, s4
	v_ashrrev_i32_e32 v213, 31, v212
	v_lshl_add_u64 v[246:247], v[212:213], 2, s[20:21]
	global_load_dword v232, v[246:247], off
	global_load_dword v231, v[246:247], off offset:64
	global_load_dword v230, v[246:247], off offset:128
	global_load_dword v229, v[246:247], off offset:192
	global_load_dword v228, v[246:247], off offset:512
	global_load_dword v227, v[246:247], off offset:576
	global_load_dword v226, v[246:247], off offset:640
	global_load_dword v225, v[246:247], off offset:704
	v_ashrrev_i32_e32 v140, 3, v214
	v_lshlrev_b64 v[144:145], 3, v[212:213]
	v_ashrrev_i32_e32 v141, 31, v140
	v_and_b32_e32 v147, 0x3fffff, v145
	v_and_b32_e32 v146, 0xfffffe00, v144
	v_lshl_add_u64 v[146:147], v[146:147], 0, v[140:141]
	v_lshlrev_b64 v[146:147], 10, v[146:147]
	v_lshlrev_b32_e32 v2, 1, v144
	v_lshl_add_u64 v[146:147], s[18:19], 0, v[146:147]
	v_and_b32_e32 v2, 0xf0, v2
	v_lshl_add_u64 v[144:145], v[146:147], 0, v[2:3]
	v_lshrrev_b32_e32 v2, 1, v148
	v_or_b32_e32 v194, 16, v212
	v_and_b32_e32 v2, 8, v2
	v_ashrrev_i32_e32 v195, 31, v194
	v_lshl_add_u64 v[144:145], v[144:145], 0, v[2:3]
	v_lshlrev_b64 v[154:155], 3, v[194:195]
	v_add_co_u32_e32 v146, vcc, s12, v144
	v_and_b32_e32 v157, 0x3fffff, v155
	v_and_b32_e32 v156, 0xfffffe00, v154
	v_addc_co_u32_e32 v147, vcc, 0, v145, vcc
	s_mov_b32 s5, 0x40000
	v_lshl_add_u64 v[156:157], v[156:157], 0, v[140:141]
	v_add_co_u32_e32 v148, vcc, s5, v144
	v_lshlrev_b64 v[156:157], 10, v[156:157]
	v_lshlrev_b32_e32 v154, 1, v154
	v_addc_co_u32_e32 v149, vcc, 0, v145, vcc
	s_mov_b32 s4, 0x60000
	v_lshl_add_u64 v[156:157], s[18:19], 0, v[156:157]
	v_and_b32_e32 v154, 0x3f0, v154
	v_mov_b32_e32 v155, v3
	v_add_co_u32_e32 v150, vcc, s4, v144
	v_lshl_add_u64 v[154:155], v[156:157], 0, v[154:155]
	s_nop 0
	v_addc_co_u32_e32 v151, vcc, 0, v145, vcc
	v_lshl_add_u64 v[154:155], v[154:155], 0, v[2:3]
	v_lshl_add_u64 v[152:153], v[194:195], 2, s[20:21]
	global_load_dwordx2 v[218:219], v[148:149], off
	global_load_dwordx2 v[216:217], v[150:151], off
	global_load_dwordx2 v[204:205], v[154:155], off
	v_add_co_u32_e32 v148, vcc, s12, v154
	v_or_b32_e32 v184, 32, v212
	s_nop 0
	v_addc_co_u32_e32 v149, vcc, 0, v155, vcc
	v_add_co_u32_e32 v150, vcc, s5, v154
	v_ashrrev_i32_e32 v185, 31, v184
	s_nop 0
	v_addc_co_u32_e32 v151, vcc, 0, v155, vcc
	v_add_co_u32_e32 v152, vcc, s4, v154
	v_or_b32_e32 v174, 48, v212
	s_nop 0
	v_addc_co_u32_e32 v153, vcc, 0, v155, vcc
	v_lshl_add_u64 v[154:155], v[184:185], 2, s[20:21]
	global_load_dwordx2 v[210:211], v[148:149], off
	global_load_dwordx2 v[208:209], v[150:151], off
	global_load_dwordx2 v[206:207], v[152:153], off
	v_lshlrev_b64 v[148:149], 3, v[184:185]
	v_and_b32_e32 v151, 0x3fffff, v149
	v_and_b32_e32 v150, 0xfffffe00, v148
	v_lshl_add_u64 v[150:151], v[150:151], 0, v[140:141]
	v_lshlrev_b64 v[150:151], 10, v[150:151]
	v_lshlrev_b32_e32 v148, 1, v148
	v_lshl_add_u64 v[150:151], s[18:19], 0, v[150:151]
	v_and_b32_e32 v148, 0x3f0, v148
	v_mov_b32_e32 v149, v3
	v_lshl_add_u64 v[148:149], v[150:151], 0, v[148:149]
	v_lshl_add_u64 v[148:149], v[148:149], 0, v[2:3]
	v_add_co_u32_e32 v150, vcc, s12, v148
	v_ashrrev_i32_e32 v175, 31, v174
	s_nop 0
	v_addc_co_u32_e32 v151, vcc, 0, v149, vcc
	v_add_co_u32_e32 v152, vcc, s5, v148
	v_lshl_add_u64 v[142:143], v[212:213], 2, s[20:21]
	s_nop 0
	v_addc_co_u32_e32 v153, vcc, 0, v149, vcc
	v_add_co_u32_e32 v154, vcc, s4, v148
	v_add_u32_e32 v164, 0x80, v212
	s_nop 0
	v_addc_co_u32_e32 v155, vcc, 0, v149, vcc
	global_load_dwordx2 v[192:193], v[148:149], off
	global_load_dwordx2 v[190:191], v[150:151], off
	global_load_dwordx2 v[188:189], v[152:153], off
	global_load_dwordx2 v[186:187], v[154:155], off
	v_lshlrev_b64 v[150:151], 3, v[174:175]
	v_and_b32_e32 v153, 0x3fffff, v151
	v_and_b32_e32 v152, 0xfffffe00, v150
	v_lshl_add_u64 v[152:153], v[152:153], 0, v[140:141]
	v_lshlrev_b64 v[152:153], 10, v[152:153]
	v_lshlrev_b32_e32 v150, 1, v150
	v_lshl_add_u64 v[152:153], s[18:19], 0, v[152:153]
	v_and_b32_e32 v150, 0x3f0, v150
	v_mov_b32_e32 v151, v3
	v_lshl_add_u64 v[150:151], v[152:153], 0, v[150:151]
	v_lshl_add_u64 v[150:151], v[150:151], 0, v[2:3]
	v_add_co_u32_e32 v152, vcc, s12, v150
	v_lshl_add_u64 v[148:149], v[174:175], 2, s[20:21]
	s_nop 0
	v_addc_co_u32_e32 v153, vcc, 0, v151, vcc
	v_add_co_u32_e32 v154, vcc, s5, v150
	v_ashrrev_i32_e32 v165, 31, v164
	s_nop 0
	v_addc_co_u32_e32 v155, vcc, 0, v151, vcc
	global_load_dwordx2 v[180:181], v[150:151], off
	global_load_dwordx2 v[178:179], v[152:153], off
	global_load_dwordx2 v[176:177], v[154:155], off
	global_load_dwordx2 v[222:223], v[144:145], off
	global_load_dwordx2 v[220:221], v[146:147], off
	v_lshlrev_b64 v[142:143], 3, v[164:165]
	v_and_b32_e32 v145, 0x3fffff, v143
	v_and_b32_e32 v144, 0xfffffe00, v142
	v_lshl_add_u64 v[144:145], v[144:145], 0, v[140:141]
	v_lshlrev_b64 v[144:145], 10, v[144:145]
	v_lshlrev_b32_e32 v142, 1, v142
	v_lshl_add_u64 v[144:145], s[18:19], 0, v[144:145]
	v_and_b32_e32 v142, 0x3f0, v142
	v_mov_b32_e32 v143, v3
	v_add_co_u32_e32 v148, vcc, s4, v150
	v_lshl_add_u64 v[142:143], v[144:145], 0, v[142:143]
	s_nop 0
	v_addc_co_u32_e32 v149, vcc, 0, v151, vcc
	v_lshl_add_u64 v[142:143], v[142:143], 0, v[2:3]
	v_add_co_u32_e32 v144, vcc, s12, v142
	v_add_u32_e32 v196, 0xb0, v212
	s_nop 0
	v_addc_co_u32_e32 v145, vcc, 0, v143, vcc
	v_add_co_u32_e32 v146, vcc, s5, v142
	v_ashrrev_i32_e32 v197, 31, v196
	s_nop 0
	v_addc_co_u32_e32 v147, vcc, 0, v143, vcc
	global_load_dwordx2 v[182:183], v[148:149], off
	global_load_dwordx2 v[170:171], v[142:143], off
	global_load_dwordx2 v[168:169], v[144:145], off
	global_load_dwordx2 v[166:167], v[146:147], off
	v_add_u32_e32 v144, 0x90, v212
	v_ashrrev_i32_e32 v145, 31, v144
	v_lshl_add_u64 v[146:147], v[144:145], 2, s[20:21]
	v_lshlrev_b64 v[144:145], 3, v[144:145]
	v_and_b32_e32 v149, 0x3fffff, v145
	v_and_b32_e32 v148, 0xfffffe00, v144
	v_lshl_add_u64 v[148:149], v[148:149], 0, v[140:141]
	v_lshlrev_b64 v[148:149], 10, v[148:149]
	v_lshlrev_b32_e32 v144, 1, v144
	v_lshl_add_u64 v[148:149], s[18:19], 0, v[148:149]
	v_and_b32_e32 v144, 0x3f0, v144
	v_mov_b32_e32 v145, v3
	v_add_co_u32_e32 v142, vcc, s4, v142
	v_lshl_add_u64 v[144:145], v[148:149], 0, v[144:145]
	s_nop 0
	v_addc_co_u32_e32 v143, vcc, 0, v143, vcc
	v_lshl_add_u64 v[144:145], v[144:145], 0, v[2:3]
	v_add_co_u32_e32 v148, vcc, s12, v144
	v_lshl_add_u64 v[198:199], v[196:197], 2, s[20:21]
	s_nop 0
	v_addc_co_u32_e32 v149, vcc, 0, v145, vcc
	global_load_dwordx2 v[172:173], v[142:143], off
	global_load_dwordx2 v[158:159], v[144:145], off
	global_load_dwordx2 v[156:157], v[148:149], off
	v_add_u32_e32 v146, 0xa0, v212
	v_ashrrev_i32_e32 v147, 31, v146
	v_lshl_add_u64 v[148:149], v[146:147], 2, s[20:21]
	v_lshlrev_b64 v[146:147], 3, v[146:147]
	v_and_b32_e32 v151, 0x3fffff, v147
	v_and_b32_e32 v150, 0xfffffe00, v146
	v_lshl_add_u64 v[150:151], v[150:151], 0, v[140:141]
	v_add_co_u32_e32 v142, vcc, s5, v144
	v_lshlrev_b64 v[150:151], 10, v[150:151]
	v_lshlrev_b32_e32 v146, 1, v146
	v_addc_co_u32_e32 v143, vcc, 0, v145, vcc
	v_lshl_add_u64 v[150:151], s[18:19], 0, v[150:151]
	v_and_b32_e32 v146, 0x3f0, v146
	v_mov_b32_e32 v147, v3
	v_add_co_u32_e32 v144, vcc, s4, v144
	v_lshl_add_u64 v[146:147], v[150:151], 0, v[146:147]
	s_nop 0
	v_addc_co_u32_e32 v145, vcc, 0, v145, vcc
	v_lshl_add_u64 v[146:147], v[146:147], 0, v[2:3]
	global_load_dwordx2 v[162:163], v[142:143], off
	global_load_dwordx2 v[160:161], v[144:145], off
	s_nop 0
	global_load_dwordx2 v[148:149], v[146:147], off
	v_add_co_u32_e32 v142, vcc, s12, v146
	s_waitcnt vmcnt(25)
	v_mul_f32_e32 v225, 0xbfb8aa3b, v225
	v_mul_f32_e32 v226, 0xbfb8aa3b, v226
	v_mul_f32_e32 v227, 0xbfb8aa3b, v227
	v_mul_f32_e32 v228, 0xbfb8aa3b, v228
	v_mul_f32_e32 v229, 0xbfb8aa3b, v229
	v_mul_f32_e32 v230, 0xbfb8aa3b, v230
	v_mul_f32_e32 v231, 0xbfb8aa3b, v231
	v_mul_f32_e32 v232, 0xbfb8aa3b, v232
	v_mul_f32_e32 v108, v231, v108
	v_addc_co_u32_e32 v143, vcc, 0, v147, vcc
	v_add_co_u32_e32 v144, vcc, s5, v146
	v_mul_f32_e32 v124, v232, v124
	s_nop 0
	v_addc_co_u32_e32 v145, vcc, 0, v147, vcc
	v_add_co_u32_e32 v146, vcc, s4, v146
	s_nop 0
	v_addc_co_u32_e32 v147, vcc, 0, v147, vcc
	global_load_dwordx2 v[154:155], v[142:143], off
	global_load_dwordx2 v[152:153], v[144:145], off
	global_load_dwordx2 v[150:151], v[146:147], off
	v_lshlrev_b64 v[142:143], 3, v[196:197]
	v_and_b32_e32 v145, 0x3fffff, v143
	v_and_b32_e32 v144, 0xfffffe00, v142
	v_lshl_add_u64 v[140:141], v[144:145], 0, v[140:141]
	v_lshlrev_b64 v[140:141], 10, v[140:141]
	v_lshlrev_b32_e32 v142, 1, v142
	v_lshl_add_u64 v[140:141], s[18:19], 0, v[140:141]
	v_and_b32_e32 v142, 0x3f0, v142
	v_mov_b32_e32 v143, v3
	v_lshl_add_u64 v[140:141], v[140:141], 0, v[142:143]
	v_lshl_add_u64 v[140:141], v[140:141], 0, v[2:3]
	v_mul_f32_e32 v2, v232, v128
	v_mul_f32_e32 v128, v232, v129
	v_exp_f32_e32 v2, v2
	v_exp_f32_e32 v129, v128
	v_mul_f32_e32 v125, v232, v125
	v_add_f32_e32 v2, 1.0, v2
	v_rcp_f32_e32 v128, v2
	v_add_f32_e32 v2, 1.0, v129
	v_mul_f32_e32 v129, v232, v130
	v_exp_f32_e32 v130, v129
	v_mul_f32_e32 v129, v232, v131
	v_exp_f32_e32 v131, v129
	v_exp_f32_e32 v124, v124
	v_exp_f32_e32 v125, v125
	v_rcp_f32_e32 v129, v2
	v_add_f32_e32 v2, 1.0, v130
	v_rcp_f32_e32 v130, v2
	v_add_f32_e32 v2, 1.0, v131
	v_rcp_f32_e32 v131, v2
	v_add_f32_e32 v2, 1.0, v124
	v_rcp_f32_e32 v124, v2
	v_add_f32_e32 v2, 1.0, v125
	v_mul_f32_e32 v125, v232, v126
	v_exp_f32_e32 v126, v125
	v_mul_f32_e32 v125, v232, v127
	v_mul_f32_e32 v120, v232, v120
	v_exp_f32_e32 v127, v125
	v_mul_f32_e32 v121, v232, v121
	v_exp_f32_e32 v120, v120
	v_exp_f32_e32 v121, v121
	v_rcp_f32_e32 v125, v2
	v_add_f32_e32 v2, 1.0, v126
	v_rcp_f32_e32 v126, v2
	v_add_f32_e32 v2, 1.0, v127
	v_rcp_f32_e32 v127, v2
	v_add_f32_e32 v2, 1.0, v120
	v_rcp_f32_e32 v120, v2
	v_add_f32_e32 v2, 1.0, v121
	v_mul_f32_e32 v121, v232, v122
	v_exp_f32_e32 v122, v121
	v_mul_f32_e32 v121, v232, v123
	v_mul_f32_e32 v116, v232, v116
	v_exp_f32_e32 v123, v121
	v_mul_f32_e32 v117, v232, v117
	v_exp_f32_e32 v116, v116
	v_exp_f32_e32 v117, v117
	v_rcp_f32_e32 v121, v2
	v_add_f32_e32 v2, 1.0, v122
	v_rcp_f32_e32 v122, v2
	v_add_f32_e32 v2, 1.0, v123
	v_rcp_f32_e32 v123, v2
	v_add_f32_e32 v2, 1.0, v116
	v_rcp_f32_e32 v116, v2
	v_add_f32_e32 v2, 1.0, v117
	v_rcp_f32_e32 v117, v2
	v_mul_f32_e32 v2, v232, v118
	v_mul_f32_e32 v118, v232, v119
	v_exp_f32_e32 v2, v2
	v_exp_f32_e32 v119, v118
	v_add_f32_e32 v2, 1.0, v2
	v_rcp_f32_e32 v118, v2
	v_add_f32_e32 v2, 1.0, v119
	v_rcp_f32_e32 v119, v2
	v_mul_f32_e32 v2, v231, v112
	v_mul_f32_e32 v112, v231, v113
	v_exp_f32_e32 v2, v2
	v_exp_f32_e32 v113, v112
	v_mul_f32_e32 v109, v231, v109
	v_add_f32_e32 v2, 1.0, v2
	v_rcp_f32_e32 v112, v2
	v_add_f32_e32 v2, 1.0, v113
	v_mul_f32_e32 v113, v231, v114
	v_exp_f32_e32 v114, v113
	v_mul_f32_e32 v113, v231, v115
	v_exp_f32_e32 v115, v113
	v_exp_f32_e32 v108, v108
	v_exp_f32_e32 v109, v109
	v_rcp_f32_e32 v113, v2
	v_add_f32_e32 v2, 1.0, v114
	v_rcp_f32_e32 v114, v2
	v_add_f32_e32 v2, 1.0, v115
	v_rcp_f32_e32 v115, v2
	v_add_f32_e32 v2, 1.0, v108
	v_rcp_f32_e32 v108, v2
	v_add_f32_e32 v2, 1.0, v109
	v_mul_f32_e32 v109, v231, v110
	v_exp_f32_e32 v110, v109
	v_mul_f32_e32 v109, v231, v111
	v_mul_f32_e32 v104, v231, v104
	v_exp_f32_e32 v111, v109
	v_mul_f32_e32 v105, v231, v105
	v_exp_f32_e32 v104, v104
	v_exp_f32_e32 v105, v105
	v_rcp_f32_e32 v109, v2
	v_add_f32_e32 v2, 1.0, v110
	v_rcp_f32_e32 v110, v2
	v_add_f32_e32 v2, 1.0, v111
	v_rcp_f32_e32 v111, v2
	v_add_f32_e32 v2, 1.0, v104
	v_rcp_f32_e32 v104, v2
	v_add_f32_e32 v2, 1.0, v105
	v_mul_f32_e32 v105, v231, v106
	v_exp_f32_e32 v106, v105
	v_mul_f32_e32 v105, v231, v107
	v_mul_f32_e32 v100, v231, v100
	v_exp_f32_e32 v107, v105
	v_mul_f32_e32 v101, v231, v101
	v_exp_f32_e32 v100, v100
	v_exp_f32_e32 v101, v101
	v_rcp_f32_e32 v105, v2
	v_add_f32_e32 v2, 1.0, v106
	v_rcp_f32_e32 v106, v2
	v_add_f32_e32 v2, 1.0, v107
	v_rcp_f32_e32 v107, v2
	v_add_f32_e32 v2, 1.0, v100
	v_rcp_f32_e32 v100, v2
	v_add_f32_e32 v2, 1.0, v101
	v_rcp_f32_e32 v101, v2
	v_mul_f32_e32 v2, v231, v102
	v_mul_f32_e32 v102, v231, v103
	v_exp_f32_e32 v2, v2
	v_exp_f32_e32 v103, v102
	v_mul_f32_e32 v92, v230, v92
	v_add_f32_e32 v2, 1.0, v2
	v_rcp_f32_e32 v102, v2
	v_add_f32_e32 v2, 1.0, v103
	v_rcp_f32_e32 v103, v2
	v_mul_f32_e32 v2, v230, v96
	v_mul_f32_e32 v96, v230, v97
	v_exp_f32_e32 v2, v2
	v_exp_f32_e32 v97, v96
	v_add_f32_e32 v2, 1.0, v2
	v_rcp_f32_e32 v96, v2
	v_add_f32_e32 v2, 1.0, v97
	v_mul_f32_e32 v97, v230, v98
	v_exp_f32_e32 v98, v97
	v_mul_f32_e32 v97, v230, v99
	v_exp_f32_e32 v99, v97
	v_mul_f32_e32 v93, v230, v93
	v_exp_f32_e32 v92, v92
	v_exp_f32_e32 v93, v93
	v_rcp_f32_e32 v97, v2
	v_add_f32_e32 v2, 1.0, v98
	v_rcp_f32_e32 v98, v2
	v_add_f32_e32 v2, 1.0, v99
	v_rcp_f32_e32 v99, v2
	v_add_f32_e32 v2, 1.0, v92
	v_rcp_f32_e32 v92, v2
	v_add_f32_e32 v2, 1.0, v93
	v_mul_f32_e32 v93, v230, v94
	v_exp_f32_e32 v94, v93
	v_mul_f32_e32 v93, v230, v95
	v_mul_f32_e32 v88, v230, v88
	v_exp_f32_e32 v95, v93
	v_mul_f32_e32 v89, v230, v89
	v_exp_f32_e32 v88, v88
	v_exp_f32_e32 v89, v89
	v_rcp_f32_e32 v93, v2
	v_add_f32_e32 v2, 1.0, v94
	v_rcp_f32_e32 v94, v2
	v_add_f32_e32 v2, 1.0, v95
	v_rcp_f32_e32 v95, v2
	v_add_f32_e32 v2, 1.0, v88
	v_rcp_f32_e32 v88, v2
	v_add_f32_e32 v2, 1.0, v89
	v_mul_f32_e32 v89, v230, v90
	v_exp_f32_e32 v90, v89
	v_mul_f32_e32 v89, v230, v91
	v_mul_f32_e32 v84, v230, v84
	v_exp_f32_e32 v91, v89
	v_mul_f32_e32 v85, v230, v85
	v_exp_f32_e32 v84, v84
	v_exp_f32_e32 v85, v85
	v_rcp_f32_e32 v89, v2
	v_add_f32_e32 v2, 1.0, v90
	v_rcp_f32_e32 v90, v2
	v_add_f32_e32 v2, 1.0, v91
	v_rcp_f32_e32 v91, v2
	v_add_f32_e32 v2, 1.0, v84
	v_rcp_f32_e32 v84, v2
	v_add_f32_e32 v2, 1.0, v85
	v_rcp_f32_e32 v85, v2
	v_mul_f32_e32 v2, v230, v86
	v_mul_f32_e32 v86, v230, v87
	v_exp_f32_e32 v2, v2
	v_exp_f32_e32 v87, v86
	v_mul_f32_e32 v76, v229, v76
	v_add_f32_e32 v2, 1.0, v2
	v_rcp_f32_e32 v86, v2
	v_add_f32_e32 v2, 1.0, v87
	v_rcp_f32_e32 v87, v2
	v_mul_f32_e32 v2, v229, v80
	v_mul_f32_e32 v80, v229, v81
	v_exp_f32_e32 v2, v2
	v_exp_f32_e32 v81, v80
	v_add_f32_e32 v2, 1.0, v2
	v_rcp_f32_e32 v80, v2
	v_add_f32_e32 v2, 1.0, v81
	v_mul_f32_e32 v81, v229, v82
	v_exp_f32_e32 v82, v81
	v_mul_f32_e32 v81, v229, v83
	v_exp_f32_e32 v83, v81
	v_mul_f32_e32 v77, v229, v77
	v_exp_f32_e32 v76, v76
	v_exp_f32_e32 v77, v77
	v_rcp_f32_e32 v81, v2
	v_add_f32_e32 v2, 1.0, v82
	v_rcp_f32_e32 v82, v2
	v_add_f32_e32 v2, 1.0, v83
	v_rcp_f32_e32 v83, v2
	v_add_f32_e32 v2, 1.0, v76
	v_rcp_f32_e32 v76, v2
	v_add_f32_e32 v2, 1.0, v77
	v_mul_f32_e32 v77, v229, v78
	v_exp_f32_e32 v78, v77
	v_mul_f32_e32 v77, v229, v79
	v_mul_f32_e32 v72, v229, v72
	v_exp_f32_e32 v79, v77
	v_mul_f32_e32 v73, v229, v73
	v_exp_f32_e32 v72, v72
	v_exp_f32_e32 v73, v73
	v_rcp_f32_e32 v77, v2
	v_add_f32_e32 v2, 1.0, v78
	v_rcp_f32_e32 v78, v2
	v_add_f32_e32 v2, 1.0, v79
	v_rcp_f32_e32 v79, v2
	v_add_f32_e32 v2, 1.0, v72
	v_rcp_f32_e32 v72, v2
	v_add_f32_e32 v2, 1.0, v73
	v_mul_f32_e32 v73, v229, v74
	v_exp_f32_e32 v74, v73
	v_mul_f32_e32 v73, v229, v75
	v_mul_f32_e32 v68, v229, v68
	v_exp_f32_e32 v75, v73
	v_mul_f32_e32 v69, v229, v69
	v_exp_f32_e32 v68, v68
	v_exp_f32_e32 v69, v69
	v_rcp_f32_e32 v73, v2
	v_add_f32_e32 v2, 1.0, v74
	v_rcp_f32_e32 v74, v2
	v_add_f32_e32 v2, 1.0, v75
	v_rcp_f32_e32 v75, v2
	v_add_f32_e32 v2, 1.0, v68
	v_rcp_f32_e32 v68, v2
	v_add_f32_e32 v2, 1.0, v69
	v_rcp_f32_e32 v69, v2
	v_mul_f32_e32 v2, v229, v70
	v_mul_f32_e32 v70, v229, v71
	v_exp_f32_e32 v2, v2
	v_exp_f32_e32 v71, v70
	v_mul_f32_e32 v60, v228, v60
	v_add_f32_e32 v2, 1.0, v2
	v_rcp_f32_e32 v70, v2
	v_add_f32_e32 v2, 1.0, v71
	v_rcp_f32_e32 v71, v2
	v_mul_f32_e32 v2, v228, v64
	v_mul_f32_e32 v64, v228, v65
	v_exp_f32_e32 v2, v2
	v_exp_f32_e32 v65, v64
	v_add_f32_e32 v2, 1.0, v2
	v_rcp_f32_e32 v64, v2
	v_add_f32_e32 v2, 1.0, v65
	v_mul_f32_e32 v65, v228, v66
	v_exp_f32_e32 v66, v65
	v_mul_f32_e32 v65, v228, v67
	v_exp_f32_e32 v67, v65
	v_mul_f32_e32 v61, v228, v61
	v_exp_f32_e32 v60, v60
	v_exp_f32_e32 v61, v61
	v_rcp_f32_e32 v65, v2
	v_add_f32_e32 v2, 1.0, v66
	v_rcp_f32_e32 v66, v2
	v_add_f32_e32 v2, 1.0, v67
	v_rcp_f32_e32 v67, v2
	v_add_f32_e32 v2, 1.0, v60
	v_rcp_f32_e32 v60, v2
	v_add_f32_e32 v2, 1.0, v61
	v_mul_f32_e32 v61, v228, v62
	v_exp_f32_e32 v62, v61
	v_mul_f32_e32 v61, v228, v63
	v_mul_f32_e32 v56, v228, v56
	v_exp_f32_e32 v63, v61
	v_mul_f32_e32 v57, v228, v57
	v_exp_f32_e32 v56, v56
	v_exp_f32_e32 v57, v57
	v_rcp_f32_e32 v61, v2
	v_add_f32_e32 v2, 1.0, v62
	v_rcp_f32_e32 v62, v2
	v_add_f32_e32 v2, 1.0, v63
	v_rcp_f32_e32 v63, v2
	v_add_f32_e32 v2, 1.0, v56
	v_rcp_f32_e32 v56, v2
	v_add_f32_e32 v2, 1.0, v57
	v_mul_f32_e32 v57, v228, v58
	v_exp_f32_e32 v58, v57
	v_mul_f32_e32 v57, v228, v59
	v_mul_f32_e32 v52, v228, v52
	v_exp_f32_e32 v59, v57
	v_mul_f32_e32 v53, v228, v53
	v_exp_f32_e32 v52, v52
	v_exp_f32_e32 v53, v53
	v_rcp_f32_e32 v57, v2
	v_add_f32_e32 v2, 1.0, v58
	v_rcp_f32_e32 v58, v2
	v_add_f32_e32 v2, 1.0, v59
	v_rcp_f32_e32 v59, v2
	v_add_f32_e32 v2, 1.0, v52
	v_rcp_f32_e32 v52, v2
	v_add_f32_e32 v2, 1.0, v53
	v_rcp_f32_e32 v53, v2
	v_mul_f32_e32 v2, v228, v54
	v_mul_f32_e32 v54, v228, v55
	v_exp_f32_e32 v2, v2
	v_exp_f32_e32 v55, v54
	v_mul_f32_e32 v44, v227, v44
	v_add_f32_e32 v2, 1.0, v2
	v_rcp_f32_e32 v54, v2
	v_add_f32_e32 v2, 1.0, v55
	v_rcp_f32_e32 v55, v2
	v_mul_f32_e32 v2, v227, v48
	v_mul_f32_e32 v48, v227, v49
	v_exp_f32_e32 v2, v2
	v_exp_f32_e32 v49, v48
	v_add_f32_e32 v2, 1.0, v2
	v_rcp_f32_e32 v48, v2
	v_add_f32_e32 v2, 1.0, v49
	v_mul_f32_e32 v49, v227, v50
	v_exp_f32_e32 v50, v49
	v_mul_f32_e32 v49, v227, v51
	v_exp_f32_e32 v51, v49
	v_mul_f32_e32 v45, v227, v45
	v_exp_f32_e32 v44, v44
	v_exp_f32_e32 v45, v45
	v_rcp_f32_e32 v49, v2
	v_add_f32_e32 v2, 1.0, v50
	v_rcp_f32_e32 v50, v2
	v_add_f32_e32 v2, 1.0, v51
	v_rcp_f32_e32 v51, v2
	v_add_f32_e32 v2, 1.0, v44
	v_rcp_f32_e32 v44, v2
	v_add_f32_e32 v2, 1.0, v45
	v_mul_f32_e32 v45, v227, v46
	v_exp_f32_e32 v46, v45
	v_mul_f32_e32 v45, v227, v47
	v_mul_f32_e32 v40, v227, v40
	v_exp_f32_e32 v47, v45
	v_mul_f32_e32 v41, v227, v41
	v_exp_f32_e32 v40, v40
	v_exp_f32_e32 v41, v41
	v_rcp_f32_e32 v45, v2
	v_add_f32_e32 v2, 1.0, v46
	v_rcp_f32_e32 v46, v2
	v_add_f32_e32 v2, 1.0, v47
	v_rcp_f32_e32 v47, v2
	v_add_f32_e32 v2, 1.0, v40
	v_rcp_f32_e32 v40, v2
	v_add_f32_e32 v2, 1.0, v41
	v_mul_f32_e32 v41, v227, v42
	v_exp_f32_e32 v42, v41
	v_mul_f32_e32 v41, v227, v43
	v_mul_f32_e32 v36, v227, v36
	v_exp_f32_e32 v43, v41
	v_mul_f32_e32 v37, v227, v37
	v_exp_f32_e32 v36, v36
	v_exp_f32_e32 v37, v37
	v_rcp_f32_e32 v41, v2
	v_add_f32_e32 v2, 1.0, v42
	v_rcp_f32_e32 v42, v2
	v_add_f32_e32 v2, 1.0, v43
	v_rcp_f32_e32 v43, v2
	v_add_f32_e32 v2, 1.0, v36
	v_rcp_f32_e32 v36, v2
	v_add_f32_e32 v2, 1.0, v37
	v_rcp_f32_e32 v37, v2
	v_mul_f32_e32 v2, v227, v38
	v_mul_f32_e32 v38, v227, v39
	v_exp_f32_e32 v2, v2
	v_exp_f32_e32 v39, v38
	s_waitcnt vmcnt(0)
	v_add_co_u32_e32 v142, vcc, s12, v140
	v_add_f32_e32 v2, 1.0, v2
	v_rcp_f32_e32 v38, v2
	v_add_f32_e32 v2, 1.0, v39
	v_rcp_f32_e32 v39, v2
	v_mul_f32_e32 v2, v226, v32
	v_mul_f32_e32 v32, v226, v33
	v_exp_f32_e32 v2, v2
	v_addc_co_u32_e32 v143, vcc, 0, v141, vcc
	v_exp_f32_e32 v33, v32
	v_add_co_u32_e32 v196, vcc, s5, v140
	v_add_f32_e32 v2, 1.0, v2
	s_nop 0
	v_addc_co_u32_e32 v197, vcc, 0, v141, vcc
	v_add_co_u32_e32 v198, vcc, s4, v140
	v_rcp_f32_e32 v32, v2
	s_nop 0
	v_addc_co_u32_e32 v199, vcc, 0, v141, vcc
	global_load_dwordx2 v[146:147], v[140:141], off
	global_load_dwordx2 v[144:145], v[142:143], off
	s_nop 0
	global_load_dwordx2 v[142:143], v[196:197], off
	global_load_dwordx2 v[140:141], v[198:199], off
	v_lshlrev_b32_e32 v196, 16, v222
	v_and_b32_e32 v197, 0xffff0000, v222
	v_add_f32_e32 v2, 1.0, v33
	v_mul_f32_e32 v33, v226, v34
	v_pk_fma_f32 v[128:129], v[128:129], v[196:197], 0 op_sel_hi:[1,1,0]
	v_lshlrev_b32_e32 v196, 16, v220
	v_and_b32_e32 v197, 0xffff0000, v220
	v_pk_fma_f32 v[124:125], v[124:125], v[196:197], v[128:129]
	v_lshlrev_b32_e32 v128, 16, v218
	v_and_b32_e32 v129, 0xffff0000, v218
	v_exp_f32_e32 v34, v33
	v_mul_f32_e32 v33, v226, v35
	v_pk_fma_f32 v[120:121], v[120:121], v[128:129], v[124:125]
	v_lshlrev_b32_e32 v124, 16, v216
	v_and_b32_e32 v125, 0xffff0000, v216
	v_mul_f32_e32 v28, v226, v28
	v_pk_fma_f32 v[116:117], v[116:117], v[124:125], v[120:121]
	v_lshlrev_b32_e32 v120, 16, v223
	v_and_b32_e32 v121, 0xffff0000, v223
	v_exp_f32_e32 v35, v33
	v_mul_f32_e32 v29, v226, v29
	v_pk_fma_f32 v[120:121], v[130:131], v[120:121], 0 op_sel_hi:[1,1,0]
	v_lshlrev_b32_e32 v124, 16, v221
	v_and_b32_e32 v125, 0xffff0000, v221
	v_exp_f32_e32 v28, v28
	v_pk_fma_f32 v[120:121], v[126:127], v[124:125], v[120:121]
	v_lshlrev_b32_e32 v124, 16, v219
	v_and_b32_e32 v125, 0xffff0000, v219
	v_exp_f32_e32 v29, v29
	v_pk_fma_f32 v[120:121], v[122:123], v[124:125], v[120:121]
	v_lshlrev_b32_e32 v122, 16, v217
	v_and_b32_e32 v123, 0xffff0000, v217
	v_rcp_f32_e32 v33, v2
	v_add_f32_e32 v2, 1.0, v34
	v_ashrrev_i32_e32 v215, 31, v214
	v_pk_fma_f32 v[118:119], v[118:119], v[122:123], v[120:121]
	v_cvt_pk_bf16_f32 v120, v116, v117
	v_lshlrev_b64 v[116:117], 11, v[212:213]
	v_rcp_f32_e32 v34, v2
	v_add_f32_e32 v2, 1.0, v35
	v_cvt_pk_bf16_f32 v121, v118, v119
	v_lshl_add_u64 v[116:117], s[14:15], 0, v[116:117]
	v_lshlrev_b64 v[118:119], 1, v[214:215]
	v_rcp_f32_e32 v35, v2
	v_add_f32_e32 v2, 1.0, v28
	v_lshl_add_u64 v[116:117], v[116:117], 0, v[118:119]
	v_rcp_f32_e32 v28, v2
	v_add_f32_e32 v2, 1.0, v29
	v_mul_f32_e32 v29, v226, v30
	global_store_dwordx2 v[116:117], v[120:121], off
	v_lshlrev_b32_e32 v120, 16, v204
	v_and_b32_e32 v121, 0xffff0000, v204
	v_pk_fma_f32 v[112:113], v[112:113], v[120:121], 0 op_sel_hi:[1,1,0]
	v_lshlrev_b32_e32 v120, 16, v210
	v_and_b32_e32 v121, 0xffff0000, v210
	v_exp_f32_e32 v30, v29
	v_mul_f32_e32 v29, v226, v31
	v_pk_fma_f32 v[108:109], v[108:109], v[120:121], v[112:113]
	v_lshlrev_b32_e32 v112, 16, v208
	v_and_b32_e32 v113, 0xffff0000, v208
	v_mul_f32_e32 v24, v226, v24
	v_pk_fma_f32 v[104:105], v[104:105], v[112:113], v[108:109]
	v_lshlrev_b32_e32 v108, 16, v206
	v_and_b32_e32 v109, 0xffff0000, v206
	v_exp_f32_e32 v31, v29
	v_mul_f32_e32 v25, v226, v25
	v_pk_fma_f32 v[100:101], v[100:101], v[108:109], v[104:105]
	v_lshlrev_b32_e32 v104, 16, v205
	v_and_b32_e32 v105, 0xffff0000, v205
	v_exp_f32_e32 v24, v24
	v_pk_fma_f32 v[104:105], v[114:115], v[104:105], 0 op_sel_hi:[1,1,0]
	v_lshlrev_b32_e32 v108, 16, v211
	v_and_b32_e32 v109, 0xffff0000, v211
	v_exp_f32_e32 v25, v25
	v_pk_fma_f32 v[104:105], v[110:111], v[108:109], v[104:105]
	v_lshlrev_b32_e32 v108, 16, v209
	v_and_b32_e32 v109, 0xffff0000, v209
	v_rcp_f32_e32 v29, v2
	v_add_f32_e32 v2, 1.0, v30
	v_pk_fma_f32 v[104:105], v[106:107], v[108:109], v[104:105]
	v_lshlrev_b32_e32 v106, 16, v207
	v_and_b32_e32 v107, 0xffff0000, v207
	v_rcp_f32_e32 v30, v2
	v_add_f32_e32 v2, 1.0, v31
	v_pk_fma_f32 v[102:103], v[102:103], v[106:107], v[104:105]
	v_rcp_f32_e32 v31, v2
	v_add_f32_e32 v2, 1.0, v24
	v_cvt_pk_bf16_f32 v100, v100, v101
	v_cvt_pk_bf16_f32 v101, v102, v103
	v_lshlrev_b64 v[102:103], 11, v[194:195]
	v_rcp_f32_e32 v24, v2
	v_add_f32_e32 v2, 1.0, v25
	v_mul_f32_e32 v25, v226, v26
	v_lshl_add_u64 v[102:103], s[14:15], 0, v[102:103]
	v_lshl_add_u64 v[102:103], v[102:103], 0, v[118:119]
	v_exp_f32_e32 v26, v25
	v_mul_f32_e32 v25, v226, v27
	global_store_dwordx2 v[102:103], v[100:101], off
	v_lshlrev_b32_e32 v100, 16, v192
	v_and_b32_e32 v101, 0xffff0000, v192
	v_mul_f32_e32 v20, v226, v20
	v_pk_fma_f32 v[96:97], v[96:97], v[100:101], 0 op_sel_hi:[1,1,0]
	v_lshlrev_b32_e32 v100, 16, v190
	v_and_b32_e32 v101, 0xffff0000, v190
	v_exp_f32_e32 v27, v25
	v_mul_f32_e32 v21, v226, v21
	v_pk_fma_f32 v[92:93], v[92:93], v[100:101], v[96:97]
	v_lshlrev_b32_e32 v96, 16, v188
	v_and_b32_e32 v97, 0xffff0000, v188
	v_exp_f32_e32 v20, v20
	v_pk_fma_f32 v[88:89], v[88:89], v[96:97], v[92:93]
	v_lshlrev_b32_e32 v92, 16, v186
	v_and_b32_e32 v93, 0xffff0000, v186
	v_exp_f32_e32 v21, v21
	v_pk_fma_f32 v[84:85], v[84:85], v[92:93], v[88:89]
	v_lshlrev_b32_e32 v88, 16, v193
	v_and_b32_e32 v89, 0xffff0000, v193
	v_rcp_f32_e32 v25, v2
	v_add_f32_e32 v2, 1.0, v26
	v_pk_fma_f32 v[88:89], v[98:99], v[88:89], 0 op_sel_hi:[1,1,0]
	v_lshlrev_b32_e32 v92, 16, v191
	v_and_b32_e32 v93, 0xffff0000, v191
	v_rcp_f32_e32 v26, v2
	v_add_f32_e32 v2, 1.0, v27
	v_pk_fma_f32 v[88:89], v[94:95], v[92:93], v[88:89]
	v_lshlrev_b32_e32 v92, 16, v189
	v_and_b32_e32 v93, 0xffff0000, v189
	v_rcp_f32_e32 v27, v2
	v_add_f32_e32 v2, 1.0, v20
	v_pk_fma_f32 v[88:89], v[90:91], v[92:93], v[88:89]
	v_lshlrev_b32_e32 v90, 16, v187
	v_and_b32_e32 v91, 0xffff0000, v187
	v_rcp_f32_e32 v20, v2
	v_add_f32_e32 v2, 1.0, v21
	v_pk_fma_f32 v[86:87], v[86:87], v[90:91], v[88:89]
	v_rcp_f32_e32 v21, v2
	v_mul_f32_e32 v2, v226, v22
	v_cvt_pk_bf16_f32 v84, v84, v85
	v_cvt_pk_bf16_f32 v85, v86, v87
	v_lshlrev_b64 v[86:87], 11, v[184:185]
	v_mul_f32_e32 v22, v226, v23
	v_lshl_add_u64 v[86:87], s[14:15], 0, v[86:87]
	v_exp_f32_e32 v2, v2
	v_lshl_add_u64 v[86:87], v[86:87], 0, v[118:119]
	v_exp_f32_e32 v23, v22
	global_store_dwordx2 v[86:87], v[84:85], off
	v_lshlrev_b32_e32 v84, 16, v180
	v_and_b32_e32 v85, 0xffff0000, v180
	v_pk_fma_f32 v[80:81], v[80:81], v[84:85], 0 op_sel_hi:[1,1,0]
	v_lshlrev_b32_e32 v84, 16, v178
	v_and_b32_e32 v85, 0xffff0000, v178
	v_pk_fma_f32 v[76:77], v[76:77], v[84:85], v[80:81]
	v_lshlrev_b32_e32 v80, 16, v176
	v_and_b32_e32 v81, 0xffff0000, v176
	v_add_f32_e32 v2, 1.0, v2
	v_pk_fma_f32 v[72:73], v[72:73], v[80:81], v[76:77]
	v_lshlrev_b32_e32 v76, 16, v182
	v_and_b32_e32 v77, 0xffff0000, v182
	v_rcp_f32_e32 v22, v2
	v_add_f32_e32 v2, 1.0, v23
	v_pk_fma_f32 v[68:69], v[68:69], v[76:77], v[72:73]
	v_lshlrev_b32_e32 v72, 16, v181
	v_and_b32_e32 v73, 0xffff0000, v181
	v_rcp_f32_e32 v23, v2
	s_waitcnt vmcnt(7)
	v_mul_f32_e32 v2, v225, v16
	v_pk_fma_f32 v[72:73], v[82:83], v[72:73], 0 op_sel_hi:[1,1,0]
	v_lshlrev_b32_e32 v76, 16, v179
	v_and_b32_e32 v77, 0xffff0000, v179
	v_mul_f32_e32 v16, v225, v17
	v_pk_fma_f32 v[72:73], v[78:79], v[76:77], v[72:73]
	v_lshlrev_b32_e32 v76, 16, v177
	v_and_b32_e32 v77, 0xffff0000, v177
	v_exp_f32_e32 v2, v2
	v_pk_fma_f32 v[72:73], v[74:75], v[76:77], v[72:73]
	v_lshlrev_b32_e32 v74, 16, v183
	v_and_b32_e32 v75, 0xffff0000, v183
	v_exp_f32_e32 v17, v16
	v_pk_fma_f32 v[70:71], v[70:71], v[74:75], v[72:73]
	v_cvt_pk_bf16_f32 v68, v68, v69
	v_cvt_pk_bf16_f32 v69, v70, v71
	v_lshlrev_b64 v[70:71], 11, v[174:175]
	v_lshl_add_u64 v[70:71], s[14:15], 0, v[70:71]
	v_add_f32_e32 v2, 1.0, v2
	v_lshl_add_u64 v[70:71], v[70:71], 0, v[118:119]
	v_rcp_f32_e32 v16, v2
	v_add_f32_e32 v2, 1.0, v17
	v_mul_f32_e32 v17, v225, v18
	global_store_dwordx2 v[70:71], v[68:69], off
	v_lshlrev_b32_e32 v68, 16, v170
	v_and_b32_e32 v69, 0xffff0000, v170
	v_pk_fma_f32 v[64:65], v[64:65], v[68:69], 0 op_sel_hi:[1,1,0]
	v_lshlrev_b32_e32 v68, 16, v168
	v_and_b32_e32 v69, 0xffff0000, v168
	v_exp_f32_e32 v18, v17
	v_mul_f32_e32 v17, v225, v19
	v_pk_fma_f32 v[60:61], v[60:61], v[68:69], v[64:65]
	v_lshlrev_b32_e32 v64, 16, v166
	v_and_b32_e32 v65, 0xffff0000, v166
	v_mul_f32_e32 v12, v225, v12
	v_pk_fma_f32 v[56:57], v[56:57], v[64:65], v[60:61]
	v_lshlrev_b32_e32 v60, 16, v172
	v_and_b32_e32 v61, 0xffff0000, v172
	v_exp_f32_e32 v19, v17
	v_mul_f32_e32 v13, v225, v13
	v_pk_fma_f32 v[52:53], v[52:53], v[60:61], v[56:57]
	v_lshlrev_b32_e32 v56, 16, v171
	v_and_b32_e32 v57, 0xffff0000, v171
	v_exp_f32_e32 v12, v12
	v_pk_fma_f32 v[56:57], v[66:67], v[56:57], 0 op_sel_hi:[1,1,0]
	v_lshlrev_b32_e32 v60, 16, v169
	v_and_b32_e32 v61, 0xffff0000, v169
	v_exp_f32_e32 v13, v13
	v_pk_fma_f32 v[56:57], v[62:63], v[60:61], v[56:57]
	v_lshlrev_b32_e32 v60, 16, v167
	v_and_b32_e32 v61, 0xffff0000, v167
	v_rcp_f32_e32 v17, v2
	v_add_f32_e32 v2, 1.0, v18
	v_pk_fma_f32 v[56:57], v[58:59], v[60:61], v[56:57]
	v_lshlrev_b32_e32 v58, 16, v173
	v_and_b32_e32 v59, 0xffff0000, v173
	v_rcp_f32_e32 v18, v2
	v_add_f32_e32 v2, 1.0, v19
	v_pk_fma_f32 v[54:55], v[54:55], v[58:59], v[56:57]
	v_rcp_f32_e32 v19, v2
	v_add_f32_e32 v2, 1.0, v12
	v_cvt_pk_bf16_f32 v52, v52, v53
	v_cvt_pk_bf16_f32 v53, v54, v55
	v_lshlrev_b64 v[54:55], 11, v[164:165]
	v_rcp_f32_e32 v12, v2
	v_add_f32_e32 v2, 1.0, v13
	v_mul_f32_e32 v13, v225, v14
	v_lshl_add_u64 v[54:55], s[14:15], 0, v[54:55]
	v_lshl_add_u64 v[54:55], v[54:55], 0, v[118:119]
	v_exp_f32_e32 v14, v13
	v_mul_f32_e32 v13, v225, v15
	global_store_dwordx2 v[54:55], v[52:53], off
	v_lshlrev_b32_e32 v52, 16, v158
	v_and_b32_e32 v53, 0xffff0000, v158
	v_mul_f32_e32 v8, v225, v8
	v_pk_fma_f32 v[48:49], v[48:49], v[52:53], 0 op_sel_hi:[1,1,0]
	v_lshlrev_b32_e32 v52, 16, v156
	v_and_b32_e32 v53, 0xffff0000, v156
	v_exp_f32_e32 v15, v13
	v_mul_f32_e32 v9, v225, v9
	v_pk_fma_f32 v[44:45], v[44:45], v[52:53], v[48:49]
	v_lshlrev_b32_e32 v48, 16, v162
	v_and_b32_e32 v49, 0xffff0000, v162
	v_exp_f32_e32 v8, v8
	v_pk_fma_f32 v[40:41], v[40:41], v[48:49], v[44:45]
	v_lshlrev_b32_e32 v44, 16, v160
	v_and_b32_e32 v45, 0xffff0000, v160
	v_exp_f32_e32 v9, v9
	v_pk_fma_f32 v[36:37], v[36:37], v[44:45], v[40:41]
	v_lshlrev_b32_e32 v40, 16, v159
	v_and_b32_e32 v41, 0xffff0000, v159
	v_rcp_f32_e32 v13, v2
	v_add_f32_e32 v2, 1.0, v14
	v_pk_fma_f32 v[40:41], v[50:51], v[40:41], 0 op_sel_hi:[1,1,0]
	v_lshlrev_b32_e32 v44, 16, v157
	v_and_b32_e32 v45, 0xffff0000, v157
	v_rcp_f32_e32 v14, v2
	v_add_f32_e32 v2, 1.0, v15
	v_pk_fma_f32 v[40:41], v[46:47], v[44:45], v[40:41]
	v_lshlrev_b32_e32 v44, 16, v163
	v_and_b32_e32 v45, 0xffff0000, v163
	v_rcp_f32_e32 v15, v2
	v_add_f32_e32 v2, 1.0, v8
	v_pk_fma_f32 v[40:41], v[42:43], v[44:45], v[40:41]
	v_lshlrev_b32_e32 v42, 16, v161
	v_and_b32_e32 v43, 0xffff0000, v161
	v_rcp_f32_e32 v8, v2
	v_add_f32_e32 v2, 1.0, v9
	v_mul_f32_e32 v9, v225, v10
	v_pk_fma_f32 v[38:39], v[38:39], v[42:43], v[40:41]
	s_mov_b32 s4, 0x48000
	v_cvt_pk_bf16_f32 v36, v36, v37
	v_cvt_pk_bf16_f32 v37, v38, v39
	v_add_co_u32_e32 v38, vcc, s4, v116
	v_exp_f32_e32 v10, v9
	v_mul_f32_e32 v9, v225, v11
	v_addc_co_u32_e32 v39, vcc, 0, v117, vcc
	v_mul_f32_e32 v4, v225, v4
	global_store_dwordx2 v[38:39], v[36:37], off
	v_lshlrev_b32_e32 v36, 16, v148
	v_and_b32_e32 v37, 0xffff0000, v148
	v_exp_f32_e32 v11, v9
	v_mul_f32_e32 v5, v225, v5
	v_pk_fma_f32 v[32:33], v[32:33], v[36:37], 0 op_sel_hi:[1,1,0]
	v_lshlrev_b32_e32 v36, 16, v154
	v_and_b32_e32 v37, 0xffff0000, v154
	v_exp_f32_e32 v4, v4
	v_pk_fma_f32 v[28:29], v[28:29], v[36:37], v[32:33]
	v_lshlrev_b32_e32 v32, 16, v152
	v_and_b32_e32 v33, 0xffff0000, v152
	v_exp_f32_e32 v5, v5
	v_pk_fma_f32 v[24:25], v[24:25], v[32:33], v[28:29]
	v_lshlrev_b32_e32 v28, 16, v150
	v_and_b32_e32 v29, 0xffff0000, v150
	v_rcp_f32_e32 v9, v2
	v_add_f32_e32 v2, 1.0, v10
	v_pk_fma_f32 v[20:21], v[20:21], v[28:29], v[24:25]
	v_lshlrev_b32_e32 v24, 16, v149
	v_and_b32_e32 v25, 0xffff0000, v149
	v_rcp_f32_e32 v10, v2
	v_add_f32_e32 v2, 1.0, v11
	v_pk_fma_f32 v[24:25], v[34:35], v[24:25], 0 op_sel_hi:[1,1,0]
	v_lshlrev_b32_e32 v28, 16, v155
	v_and_b32_e32 v29, 0xffff0000, v155
	v_rcp_f32_e32 v11, v2
	v_add_f32_e32 v2, 1.0, v4
	v_pk_fma_f32 v[24:25], v[30:31], v[28:29], v[24:25]
	v_lshlrev_b32_e32 v28, 16, v153
	v_and_b32_e32 v29, 0xffff0000, v153
	v_rcp_f32_e32 v4, v2
	v_add_f32_e32 v2, 1.0, v5
	v_pk_fma_f32 v[24:25], v[26:27], v[28:29], v[24:25]
	v_lshlrev_b32_e32 v26, 16, v151
	v_and_b32_e32 v27, 0xffff0000, v151
	v_rcp_f32_e32 v5, v2
	v_mul_f32_e32 v2, v225, v6
	v_pk_fma_f32 v[22:23], v[22:23], v[26:27], v[24:25]
	s_mov_b32 s4, 0x50000
	v_mul_f32_e32 v6, v225, v7
	v_cvt_pk_bf16_f32 v20, v20, v21
	v_cvt_pk_bf16_f32 v21, v22, v23
	v_add_co_u32_e32 v22, vcc, s4, v116
	v_exp_f32_e32 v2, v2
	v_addc_co_u32_e32 v23, vcc, 0, v117, vcc
	v_exp_f32_e32 v7, v6
	global_store_dwordx2 v[22:23], v[20:21], off
	s_waitcnt vmcnt(10)
	v_lshlrev_b32_e32 v20, 16, v146
	v_and_b32_e32 v21, 0xffff0000, v146
	v_pk_fma_f32 v[16:17], v[16:17], v[20:21], 0 op_sel_hi:[1,1,0]
	s_waitcnt vmcnt(9)
	v_lshlrev_b32_e32 v20, 16, v144
	v_and_b32_e32 v21, 0xffff0000, v144
	v_pk_fma_f32 v[12:13], v[12:13], v[20:21], v[16:17]
	s_waitcnt vmcnt(8)
	v_lshlrev_b32_e32 v16, 16, v142
	v_and_b32_e32 v17, 0xffff0000, v142
	v_add_f32_e32 v2, 1.0, v2
	v_pk_fma_f32 v[8:9], v[8:9], v[16:17], v[12:13]
	s_waitcnt vmcnt(7)
	v_lshlrev_b32_e32 v12, 16, v140
	v_and_b32_e32 v13, 0xffff0000, v140
	v_rcp_f32_e32 v6, v2
	v_add_f32_e32 v2, 1.0, v7
	v_pk_fma_f32 v[4:5], v[4:5], v[12:13], v[8:9]
	v_rcp_f32_e32 v7, v2
	v_lshlrev_b32_e32 v8, 16, v147
	v_and_b32_e32 v9, 0xffff0000, v147
	v_pk_fma_f32 v[8:9], v[18:19], v[8:9], 0 op_sel_hi:[1,1,0]
	v_lshlrev_b32_e32 v12, 16, v145
	v_and_b32_e32 v13, 0xffff0000, v145
	v_pk_fma_f32 v[8:9], v[14:15], v[12:13], v[8:9]
	v_lshlrev_b32_e32 v12, 16, v143
	v_and_b32_e32 v13, 0xffff0000, v143
	v_pk_fma_f32 v[8:9], v[10:11], v[12:13], v[8:9]
	v_lshlrev_b32_e32 v10, 16, v141
	v_and_b32_e32 v11, 0xffff0000, v141
	v_pk_fma_f32 v[6:7], v[6:7], v[10:11], v[8:9]
	v_cvt_pk_bf16_f32 v4, v4, v5
	v_cvt_pk_bf16_f32 v5, v6, v7
	v_add_co_u32_e32 v6, vcc, 0x58000, v116
	s_mov_b64 s[4:5], -1
	s_nop 0
	v_addc_co_u32_e32 v7, vcc, 0, v117, vcc
	s_andn2_b64 vcc, exec, s[38:39]
	s_mov_b32 s77, 0xc000
	s_mov_b32 s76, 0xe000
	s_movk_i32 s75, 0x3400
	v_readlane_b32 s74, v255, 38
	global_store_dwordx2 v[6:7], v[4:5], off
	s_cbranch_vccnz .LBB0_1036
	s_andn2_b64 vcc, exec, s[10:11]
	s_cbranch_vccnz .LBB0_1035
	s_barrier
	s_branch .LBB0_1035

.LBB0_1380:
	s_add_u32 s4, s40, s50
	s_addc_u32 s5, s41, s51
	s_add_u32 s75, s4, 0x100
	s_addc_u32 s76, s5, 0
	s_add_u32 s52, s72, s50
	s_addc_u32 s53, s73, s51
	s_add_u32 s4, s4, 0x180
	s_addc_u32 s5, s5, 0
	s_add_i32 s77, 0, 0x10000
	s_add_i32 s78, 0, 0x14000
	v_add_u32_e32 v2, s77, v160
	ds_read_b128 v[148:151], v2
	ds_read_b128 v[152:155], v2 offset:1024
	ds_read_b128 v[156:159], v2 offset:2048
	ds_read_b128 v[162:165], v2 offset:3072
	v_add_u32_e32 v2, s78, v160
	ds_read_b128 v[166:169], v2
	ds_read_b128 v[170:173], v2 offset:1024
	ds_read_b128 v[174:177], v2 offset:2048
	ds_read_b128 v[178:181], v2 offset:3072
	s_cmpk_eq_i32 s50, 0x700
	s_cselect_b32 s13, s71, s5
	s_cselect_b32 s12, s70, s4
	s_cselect_b32 s53, s37, s53
	s_cselect_b32 s52, s69, s52
	s_cselect_b32 s5, s43, s76
	s_cselect_b32 s4, s68, s75
	v_lshl_add_u64 v[198:199], v[144:145], 0, s[50:51]
	s_add_i32 m0, s17, 0xc000
	ds_read_b128 v[182:185], v161
	ds_read_b128 v[186:189], v161 offset:1024
	ds_read_b128 v[190:193], v161 offset:2048
	ds_read_b128 v[194:197], v161 offset:3072
	ds_read_b128 v[204:207], v161 offset:4096
	ds_read_b128 v[208:211], v161 offset:5120
	ds_read_b128 v[212:215], v161 offset:6144
	ds_read_b128 v[216:219], v161 offset:7168
	global_load_lds_dwordx4 v[198:199], off
	v_lshl_add_u64 v[198:199], v[146:147], 0, s[50:51]
	s_add_i32 m0, s17, 0xe000
	s_nop 0
	global_load_lds_dwordx4 v[198:199], off
	s_waitcnt vmcnt(8)
	s_waitcnt lgkmcnt(0)
	s_barrier
	s_setprio 1
	v_mfma_f32_16x16x32_bf16 v[128:131], v[148:151], v[182:185], v[128:131]
	v_mfma_f32_16x16x32_bf16 v[124:127], v[156:159], v[182:185], v[124:127]
	v_mfma_f32_16x16x32_bf16 v[112:115], v[148:151], v[190:193], v[112:115]
	v_mfma_f32_16x16x32_bf16 v[108:111], v[156:159], v[190:193], v[108:111]
	v_mfma_f32_16x16x32_bf16 v[96:99], v[148:151], v[204:207], v[96:99]
	v_mfma_f32_16x16x32_bf16 v[92:95], v[156:159], v[204:207], v[92:95]
	v_mfma_f32_16x16x32_bf16 v[80:83], v[148:151], v[212:215], v[80:83]
	v_mfma_f32_16x16x32_bf16 v[76:79], v[156:159], v[212:215], v[76:79]
	v_mfma_f32_16x16x32_bf16 v[128:131], v[152:155], v[186:189], v[128:131]
	v_mfma_f32_16x16x32_bf16 v[124:127], v[162:165], v[186:189], v[124:127]
	v_mfma_f32_16x16x32_bf16 v[112:115], v[152:155], v[194:197], v[112:115]
	v_mfma_f32_16x16x32_bf16 v[108:111], v[162:165], v[194:197], v[108:111]
	v_mfma_f32_16x16x32_bf16 v[96:99], v[152:155], v[208:211], v[96:99]
	v_mfma_f32_16x16x32_bf16 v[92:95], v[162:165], v[208:211], v[92:95]
	v_mfma_f32_16x16x32_bf16 v[80:83], v[152:155], v[216:219], v[80:83]
	v_mfma_f32_16x16x32_bf16 v[76:79], v[162:165], v[216:219], v[76:79]
	v_mfma_f32_16x16x32_bf16 v[120:123], v[166:169], v[182:185], v[120:123]
	v_mfma_f32_16x16x32_bf16 v[116:119], v[174:177], v[182:185], v[116:119]
	v_mfma_f32_16x16x32_bf16 v[104:107], v[166:169], v[190:193], v[104:107]
	v_mfma_f32_16x16x32_bf16 v[100:103], v[174:177], v[190:193], v[100:103]
	v_mfma_f32_16x16x32_bf16 v[88:91], v[166:169], v[204:207], v[88:91]
	v_mfma_f32_16x16x32_bf16 v[84:87], v[174:177], v[204:207], v[84:87]
	v_mfma_f32_16x16x32_bf16 v[72:75], v[166:169], v[212:215], v[72:75]
	v_mfma_f32_16x16x32_bf16 v[68:71], v[174:177], v[212:215], v[68:71]
	v_mfma_f32_16x16x32_bf16 v[120:123], v[170:173], v[186:189], v[120:123]
	v_mfma_f32_16x16x32_bf16 v[116:119], v[178:181], v[186:189], v[116:119]
	v_mfma_f32_16x16x32_bf16 v[104:107], v[170:173], v[194:197], v[104:107]
	v_mfma_f32_16x16x32_bf16 v[100:103], v[178:181], v[194:197], v[100:103]
	v_mfma_f32_16x16x32_bf16 v[88:91], v[170:173], v[208:211], v[88:91]
	v_mfma_f32_16x16x32_bf16 v[84:87], v[178:181], v[208:211], v[84:87]
	v_mfma_f32_16x16x32_bf16 v[72:75], v[170:173], v[216:219], v[72:75]
	v_mfma_f32_16x16x32_bf16 v[68:71], v[178:181], v[216:219], v[68:71]
	s_setprio 0
	s_barrier
	s_add_i32 s75, s77, s16
	v_lshl_add_u64 v[198:199], s[52:53], 0, v[136:137]
	s_mov_b32 m0, s75
	ds_read_b128 v[182:185], v161 offset:16384
	ds_read_b128 v[186:189], v161 offset:17408
	ds_read_b128 v[190:193], v161 offset:18432
	ds_read_b128 v[194:197], v161 offset:19456
	ds_read_b128 v[204:207], v161 offset:20480
	ds_read_b128 v[208:211], v161 offset:21504
	ds_read_b128 v[212:215], v161 offset:22528
	ds_read_b128 v[216:219], v161 offset:23552
	global_load_lds_dwordx4 v[198:199], off
	s_add_i32 m0, s75, 0x2000
	s_add_u32 s76, s52, 0x40000
	v_lshl_add_u64 v[220:221], s[52:53], 0, v[132:133]
	s_addc_u32 s77, s53, 0
	s_add_i32 s75, s78, s16
	global_load_lds_dwordx4 v[220:221], off
	v_lshl_add_u64 v[222:223], s[76:77], 0, v[136:137]
	s_mov_b32 m0, s75
	s_nop 0
	global_load_lds_dwordx4 v[222:223], off
	v_lshl_add_u64 v[222:223], s[76:77], 0, v[132:133]
	s_add_i32 m0, s75, 0x2000
	s_nop 0
	global_load_lds_dwordx4 v[222:223], off
	v_lshl_add_u64 v[222:223], s[4:5], 0, v[138:139]
	s_mov_b32 m0, s17
	s_nop 0
	global_load_lds_dwordx4 v[222:223], off
	v_lshl_add_u64 v[222:223], s[4:5], 0, v[134:135]
	s_mov_b32 m0, s46
	s_nop 0
	global_load_lds_dwordx4 v[222:223], off
	s_waitcnt vmcnt(8)
	s_waitcnt lgkmcnt(0)
	s_barrier
	s_setprio 1
	v_mfma_f32_16x16x32_bf16 v[64:67], v[148:151], v[182:185], v[64:67]
	v_mfma_f32_16x16x32_bf16 v[60:63], v[156:159], v[182:185], v[60:63]
	v_mfma_f32_16x16x32_bf16 v[48:51], v[148:151], v[190:193], v[48:51]
	v_mfma_f32_16x16x32_bf16 v[44:47], v[156:159], v[190:193], v[44:47]
	v_mfma_f32_16x16x32_bf16 v[32:35], v[148:151], v[204:207], v[32:35]
	v_mfma_f32_16x16x32_bf16 v[28:31], v[156:159], v[204:207], v[28:31]
	v_mfma_f32_16x16x32_bf16 v[16:19], v[148:151], v[212:215], v[16:19]
	v_mfma_f32_16x16x32_bf16 v[12:15], v[156:159], v[212:215], v[12:15]
	v_mfma_f32_16x16x32_bf16 v[64:67], v[152:155], v[186:189], v[64:67]
	v_mfma_f32_16x16x32_bf16 v[60:63], v[162:165], v[186:189], v[60:63]
	v_mfma_f32_16x16x32_bf16 v[48:51], v[152:155], v[194:197], v[48:51]
	v_mfma_f32_16x16x32_bf16 v[44:47], v[162:165], v[194:197], v[44:47]
	v_mfma_f32_16x16x32_bf16 v[32:35], v[152:155], v[208:211], v[32:35]
	v_mfma_f32_16x16x32_bf16 v[28:31], v[162:165], v[208:211], v[28:31]
	v_mfma_f32_16x16x32_bf16 v[16:19], v[152:155], v[216:219], v[16:19]
	v_mfma_f32_16x16x32_bf16 v[12:15], v[162:165], v[216:219], v[12:15]
	v_mfma_f32_16x16x32_bf16 v[56:59], v[166:169], v[182:185], v[56:59]
	v_mfma_f32_16x16x32_bf16 v[52:55], v[174:177], v[182:185], v[52:55]
	v_mfma_f32_16x16x32_bf16 v[40:43], v[166:169], v[190:193], v[40:43]
	v_mfma_f32_16x16x32_bf16 v[36:39], v[174:177], v[190:193], v[36:39]
	v_mfma_f32_16x16x32_bf16 v[24:27], v[166:169], v[204:207], v[24:27]
	v_mfma_f32_16x16x32_bf16 v[20:23], v[174:177], v[204:207], v[20:23]
	v_mfma_f32_16x16x32_bf16 v[8:11], v[166:169], v[212:215], v[8:11]
	v_mfma_f32_16x16x32_bf16 v[4:7], v[174:177], v[212:215], v[4:7]
	v_mfma_f32_16x16x32_bf16 v[56:59], v[170:173], v[186:189], v[56:59]
	v_mfma_f32_16x16x32_bf16 v[52:55], v[178:181], v[186:189], v[52:55]
	v_mfma_f32_16x16x32_bf16 v[40:43], v[170:173], v[194:197], v[40:43]
	v_mfma_f32_16x16x32_bf16 v[36:39], v[178:181], v[194:197], v[36:39]
	v_mfma_f32_16x16x32_bf16 v[24:27], v[170:173], v[208:211], v[24:27]
	v_mfma_f32_16x16x32_bf16 v[20:23], v[178:181], v[208:211], v[20:23]
	v_mfma_f32_16x16x32_bf16 v[8:11], v[170:173], v[216:219], v[8:11]
	v_mfma_f32_16x16x32_bf16 v[4:7], v[178:181], v[216:219], v[4:7]
	s_setprio 0
	s_barrier
	s_add_i32 s75, 0, 0x18000
	v_add_u32_e32 v2, s75, v160
	s_add_i32 s76, 0, 0x1c000
	ds_read_b128 v[148:151], v2
	ds_read_b128 v[152:155], v2 offset:1024
	ds_read_b128 v[156:159], v2 offset:2048
	ds_read_b128 v[162:165], v2 offset:3072
	v_add_u32_e32 v2, s76, v160
	ds_read_b128 v[166:169], v2
	ds_read_b128 v[170:173], v2 offset:1024
	ds_read_b128 v[174:177], v2 offset:2048
	ds_read_b128 v[178:181], v2 offset:3072
	s_add_u32 s4, s4, 0x40000
	s_addc_u32 s5, s5, 0
	s_mov_b32 m0, s47
	v_lshl_add_u64 v[222:223], s[4:5], 0, v[138:139]
	ds_read_b128 v[182:185], v161 offset:32768
	ds_read_b128 v[186:189], v161 offset:33792
	ds_read_b128 v[190:193], v161 offset:34816
	ds_read_b128 v[194:197], v161 offset:35840
	ds_read_b128 v[204:207], v161 offset:36864
	ds_read_b128 v[208:211], v161 offset:37888
	ds_read_b128 v[212:215], v161 offset:38912
	ds_read_b128 v[216:219], v161 offset:39936
	global_load_lds_dwordx4 v[222:223], off
	v_lshl_add_u64 v[222:223], s[4:5], 0, v[134:135]
	s_mov_b32 m0, s56
	s_nop 0
	global_load_lds_dwordx4 v[222:223], off
	s_waitcnt vmcnt(8)
	s_waitcnt lgkmcnt(0)
	s_barrier
	s_setprio 1
	v_mfma_f32_16x16x32_bf16 v[128:131], v[148:151], v[182:185], v[128:131]
	v_mfma_f32_16x16x32_bf16 v[124:127], v[156:159], v[182:185], v[124:127]
	v_mfma_f32_16x16x32_bf16 v[112:115], v[148:151], v[190:193], v[112:115]
	v_mfma_f32_16x16x32_bf16 v[108:111], v[156:159], v[190:193], v[108:111]
	v_mfma_f32_16x16x32_bf16 v[96:99], v[148:151], v[204:207], v[96:99]
	v_mfma_f32_16x16x32_bf16 v[92:95], v[156:159], v[204:207], v[92:95]
	v_mfma_f32_16x16x32_bf16 v[80:83], v[148:151], v[212:215], v[80:83]
	v_mfma_f32_16x16x32_bf16 v[76:79], v[156:159], v[212:215], v[76:79]
	v_mfma_f32_16x16x32_bf16 v[128:131], v[152:155], v[186:189], v[128:131]
	v_mfma_f32_16x16x32_bf16 v[124:127], v[162:165], v[186:189], v[124:127]
	v_mfma_f32_16x16x32_bf16 v[112:115], v[152:155], v[194:197], v[112:115]
	v_mfma_f32_16x16x32_bf16 v[108:111], v[162:165], v[194:197], v[108:111]
	v_mfma_f32_16x16x32_bf16 v[96:99], v[152:155], v[208:211], v[96:99]
	v_mfma_f32_16x16x32_bf16 v[92:95], v[162:165], v[208:211], v[92:95]
	v_mfma_f32_16x16x32_bf16 v[80:83], v[152:155], v[216:219], v[80:83]
	v_mfma_f32_16x16x32_bf16 v[76:79], v[162:165], v[216:219], v[76:79]
	v_mfma_f32_16x16x32_bf16 v[120:123], v[166:169], v[182:185], v[120:123]
	v_mfma_f32_16x16x32_bf16 v[116:119], v[174:177], v[182:185], v[116:119]
	v_mfma_f32_16x16x32_bf16 v[104:107], v[166:169], v[190:193], v[104:107]
	v_mfma_f32_16x16x32_bf16 v[100:103], v[174:177], v[190:193], v[100:103]
	v_mfma_f32_16x16x32_bf16 v[88:91], v[166:169], v[204:207], v[88:91]
	v_mfma_f32_16x16x32_bf16 v[84:87], v[174:177], v[204:207], v[84:87]
	v_mfma_f32_16x16x32_bf16 v[72:75], v[166:169], v[212:215], v[72:75]
	v_mfma_f32_16x16x32_bf16 v[68:71], v[174:177], v[212:215], v[68:71]
	v_mfma_f32_16x16x32_bf16 v[120:123], v[170:173], v[186:189], v[120:123]
	v_mfma_f32_16x16x32_bf16 v[116:119], v[178:181], v[186:189], v[116:119]
	v_mfma_f32_16x16x32_bf16 v[104:107], v[170:173], v[194:197], v[104:107]
	v_mfma_f32_16x16x32_bf16 v[100:103], v[178:181], v[194:197], v[100:103]
	v_mfma_f32_16x16x32_bf16 v[88:91], v[170:173], v[208:211], v[88:91]
	v_mfma_f32_16x16x32_bf16 v[84:87], v[178:181], v[208:211], v[84:87]
	v_mfma_f32_16x16x32_bf16 v[72:75], v[170:173], v[216:219], v[72:75]
	v_mfma_f32_16x16x32_bf16 v[68:71], v[178:181], v[216:219], v[68:71]
	s_setprio 0
	s_barrier
	s_add_i32 s4, s75, s16
	v_lshl_add_u64 v[198:199], v[198:199], 0, s[34:35]
	s_mov_b32 m0, s4
	ds_read_b128 v[182:185], v161 offset:49152
	ds_read_b128 v[186:189], v161 offset:50176
	ds_read_b128 v[190:193], v161 offset:51200
	ds_read_b128 v[194:197], v161 offset:52224
	ds_read_b128 v[204:207], v161 offset:53248
	ds_read_b128 v[208:211], v161 offset:54272
	ds_read_b128 v[212:215], v161 offset:55296
	ds_read_b128 v[216:219], v161 offset:56320
	global_load_lds_dwordx4 v[198:199], off
	s_add_i32 m0, s4, 0x2000
	s_add_u32 s4, s52, 0x40080
	v_lshl_add_u64 v[198:199], v[220:221], 0, s[34:35]
	s_addc_u32 s5, s53, 0
	s_add_i32 s52, s76, s16
	global_load_lds_dwordx4 v[198:199], off
	v_lshl_add_u64 v[198:199], s[4:5], 0, v[136:137]
	s_mov_b32 m0, s52
	s_nop 0
	global_load_lds_dwordx4 v[198:199], off
	v_lshl_add_u64 v[198:199], s[4:5], 0, v[132:133]
	s_add_i32 m0, s52, 0x2000
	s_nop 0
	global_load_lds_dwordx4 v[198:199], off
	v_lshl_add_u64 v[198:199], s[12:13], 0, v[138:139]
	s_mov_b32 m0, s61
	s_nop 0
	global_load_lds_dwordx4 v[198:199], off
	v_lshl_add_u64 v[198:199], s[12:13], 0, v[134:135]
	s_mov_b32 m0, s62
	s_nop 0
	global_load_lds_dwordx4 v[198:199], off
	s_waitcnt vmcnt(8)
	s_waitcnt lgkmcnt(0)
	s_barrier
	s_setprio 1
	v_mfma_f32_16x16x32_bf16 v[64:67], v[148:151], v[182:185], v[64:67]
	v_mfma_f32_16x16x32_bf16 v[60:63], v[156:159], v[182:185], v[60:63]
	v_mfma_f32_16x16x32_bf16 v[48:51], v[148:151], v[190:193], v[48:51]
	v_mfma_f32_16x16x32_bf16 v[44:47], v[156:159], v[190:193], v[44:47]
	v_mfma_f32_16x16x32_bf16 v[32:35], v[148:151], v[204:207], v[32:35]
	v_mfma_f32_16x16x32_bf16 v[28:31], v[156:159], v[204:207], v[28:31]
	v_mfma_f32_16x16x32_bf16 v[16:19], v[148:151], v[212:215], v[16:19]
	v_mfma_f32_16x16x32_bf16 v[12:15], v[156:159], v[212:215], v[12:15]
	v_mfma_f32_16x16x32_bf16 v[64:67], v[152:155], v[186:189], v[64:67]
	v_mfma_f32_16x16x32_bf16 v[60:63], v[162:165], v[186:189], v[60:63]
	v_mfma_f32_16x16x32_bf16 v[48:51], v[152:155], v[194:197], v[48:51]
	v_mfma_f32_16x16x32_bf16 v[44:47], v[162:165], v[194:197], v[44:47]
	v_mfma_f32_16x16x32_bf16 v[32:35], v[152:155], v[208:211], v[32:35]
	v_mfma_f32_16x16x32_bf16 v[28:31], v[162:165], v[208:211], v[28:31]
	v_mfma_f32_16x16x32_bf16 v[16:19], v[152:155], v[216:219], v[16:19]
	v_mfma_f32_16x16x32_bf16 v[12:15], v[162:165], v[216:219], v[12:15]
	v_mfma_f32_16x16x32_bf16 v[56:59], v[166:169], v[182:185], v[56:59]
	v_mfma_f32_16x16x32_bf16 v[52:55], v[174:177], v[182:185], v[52:55]
	v_mfma_f32_16x16x32_bf16 v[40:43], v[166:169], v[190:193], v[40:43]
	v_mfma_f32_16x16x32_bf16 v[36:39], v[174:177], v[190:193], v[36:39]
	v_mfma_f32_16x16x32_bf16 v[24:27], v[166:169], v[204:207], v[24:27]
	v_mfma_f32_16x16x32_bf16 v[20:23], v[174:177], v[204:207], v[20:23]
	v_mfma_f32_16x16x32_bf16 v[8:11], v[166:169], v[212:215], v[8:11]
	v_mfma_f32_16x16x32_bf16 v[4:7], v[174:177], v[212:215], v[4:7]
	v_mfma_f32_16x16x32_bf16 v[56:59], v[170:173], v[186:189], v[56:59]
	v_mfma_f32_16x16x32_bf16 v[52:55], v[178:181], v[186:189], v[52:55]
	v_mfma_f32_16x16x32_bf16 v[40:43], v[170:173], v[194:197], v[40:43]
	v_mfma_f32_16x16x32_bf16 v[36:39], v[178:181], v[194:197], v[36:39]
	v_mfma_f32_16x16x32_bf16 v[24:27], v[170:173], v[208:211], v[24:27]
	v_mfma_f32_16x16x32_bf16 v[20:23], v[178:181], v[208:211], v[20:23]
	v_mfma_f32_16x16x32_bf16 v[8:11], v[170:173], v[216:219], v[8:11]
	v_mfma_f32_16x16x32_bf16 v[4:7], v[178:181], v[216:219], v[4:7]
	s_setprio 0
	s_barrier
	s_add_i32 s74, s74, 2
	s_add_u32 s50, s50, 0x100
	s_addc_u32 s51, s51, 0
	s_cmp_gt_u32 s74, 13
	s_cbranch_scc0 .LBB0_1380
	s_and_b64 vcc, exec, s[22:23]
	s_cbranch_vccz .LBB0_1383
	s_barrier
